# P5 step loop: LDS-DMA issue uses SGPR block base + 32-bit lane offsets (saddr form) instead of 64-bit VALU address chains, on top of v28
# speedup vs baseline: 1.0098x; 1.0029x over previous
; #define LAS __attribute__((address_space(3)))
; __device__ __forceinline__ int ta_swk(int r) { return (((r >> 3) & 3) << 2) | (r & 3); }
; #define TA_ISSUE(n_) do { if (DRY == 2) break; const int _j = TA_BLK(n_); ta_issue(lds, (n_) & 3, Kbg + (size_t)_j * 64 * 128, Vbg + (size_t)_j * 8192, w, lane); } while (0)
; __device__ __forceinline__ void ta_issue(LAS unsigned char* lds, int bufi, const bf16_t* Kb, const bf16_t* Vb, int w, int lane, bool konly = false) {
;     LAS unsigned char* kb = lds + bufi * 32768; LAS unsigned char* vb = kb + 16384;
; #pragma unroll
;     for (int q = 0; q < 2; ++q) { const int r = 8 * w + 4 * q + (lane >> 4), s = lane & 15;
;         __builtin_amdgcn_global_load_lds((const unsigned*)(Kb + (size_t)r * 128 + ((s ^ ta_swk(r)) * 8)), (LAS unsigned*)(kb + (8 * w + 4 * q) * 256), 16, 0, 0); }
;     if (konly) return;
; #pragma unroll
;     for (int q = 0; q < 2; ++q) { const int d = 16 * w + 8 * q + (lane >> 3), s = lane & 7;
;         __builtin_amdgcn_global_load_lds((const unsigned*)(Vb + (size_t)d * 64 + ((s ^ ((d >> 1) & 7)) * 8)), (LAS unsigned*)(vb + (16 * w + 8 * q) * 128), 16, 0, 0); }
; }
;     ...
;         if (MODE == MODE_SEL) {
;             TA_ISSUE(0); if (nblk > 1) TA_ISSUE(1);
;             for (int n = 0; n < nblk; n += 2) {
;                 asm volatile("s_waitcnt vmcnt(0)" ::: "memory"); __syncthreads();
;                 if (n + 2 < nblk) TA_ISSUE(n + 2);
;                 if (n + 3 < nblk) TA_ISSUE(n + 3);
.LBB0_695:
	s_waitcnt vmcnt(0)
	s_add_i32 s0, s77, 1
	s_cmp_ge_i32 s0, s74
	s_waitcnt lgkmcnt(0)
	s_barrier
	s_cbranch_scc1 .LBB0_697
	s_lshl_b32 s92, s84, 14
	s_add_u32 s94, s2, s92
	s_addc_u32 s95, s3, 0
	s_add_u32 s96, s48, s92
	s_addc_u32 s97, s49, 0
	s_add_i32 s0, s75, 0x10000
	s_and_b32 s0, s0, 0x10000
	s_add_i32 s0, s0, 0
	s_add_i32 s1, s0, s55
	s_waitcnt lgkmcnt(0)
	v_add_u32_e32 v98, v202, v200
	v_add_u32_e32 v99, v204, v200
	v_add_u32_e32 v100, v206, v214
	v_add_u32_e32 v101, v208, v216
	s_mov_b32 m0, s1
	s_nop 0
	global_load_lds_dwordx4 v98, s[94:95]
	s_add_i32 m0, s0, s56
	s_nop 0
	global_load_lds_dwordx4 v99, s[94:95]
	s_add_i32 m0, s1, 0x4000
	s_add_i32 s0, s0, s57
	global_load_lds_dwordx4 v100, s[96:97]
	s_add_i32 m0, s0, 0x4000
	s_nop 0
	global_load_lds_dwordx4 v101, s[96:97]
.LBB0_697:
	s_add_i32 s76, s77, 2
	s_cmp_ge_i32 s76, s74
	s_cbranch_scc1 .LBB0_699
	s_lshl_b32 s92, s85, 14
	s_add_u32 s94, s2, s92
	s_addc_u32 s95, s3, 0
	s_add_u32 s96, s48, s92
	s_addc_u32 s97, s49, 0
	s_add_i32 s0, s75, 0x18000
	s_and_b32 s0, s0, 0x18000
	s_add_i32 s0, s0, 0
	s_add_i32 s1, s0, s55
	s_waitcnt lgkmcnt(0)
	s_mov_b32 m0, s1
	s_nop 0
	global_load_lds_dwordx4 v98, s[94:95]
	s_add_i32 m0, s0, s56
	s_nop 0
	global_load_lds_dwordx4 v99, s[94:95]
	s_add_i32 m0, s1, 0x4000
	s_add_i32 s0, s0, s57
	global_load_lds_dwordx4 v100, s[96:97]
	s_add_i32 m0, s0, 0x4000
	s_nop 0
	global_load_lds_dwordx4 v101, s[96:97]
